# v37
# baseline (speedup 1.0000x reference)
.Lprio_half:
	ds_read_b128 v[0:3], v72 offset:12288
	ds_read_b128 v[4:7], v71 offset:42752
	ds_read_b128 v[8:11], v72 offset:13312
	ds_read_b128 v[12:15], v72 offset:14336
	ds_read_b128 v[34:37], v72 offset:15360
	ds_read_b128 v[44:47], v71 offset:42816
	v_cvt_pk_f16_f32 v30, v52, v53
	v_cvt_pk_f16_f32 v26, v26, v27
	v_cvt_pk_f16_f32 v31, v54, v55
	s_waitcnt lgkmcnt(4)
	v_mfma_f32_16x16x32_f16 v[48:51], v[0:3], v[22:25], v[4:7]
	v_cvt_pk_f16_f32 v32, v56, v57
	v_cvt_pk_f16_f32 v33, v58, v59
	v_cvt_pk_f16_f32 v27, v28, v29
	v_mfma_f32_16x16x32_f16 v[0:3], v[0:3], v[18:21], v[4:7]
	v_cvt_pk_f16_f32 v28, v16, v17
	v_cvt_pk_f16_f32 v29, v60, v61
	s_add_i32 s11, s9, s12
	s_waitcnt lgkmcnt(3)
	v_mfma_f32_16x16x32_f16 v[48:51], v[8:11], v[30:33], v[48:51]
	s_cmp_lt_i32 s11, 0x8000
	s_cselect_b32 s10, s11, s10
	s_ashr_i32 s11, s10, 31
	v_mfma_f32_16x16x32_f16 v[52:55], v[8:11], v[26:29], v[0:3]
	ds_read_b128 v[4:7], v72 offset:17408
	ds_read_b128 v[8:11], v71 offset:42880
	s_lshl_b64 s[10:11], s[10:11], 12
	s_add_u32 s10, s10, s36
	s_addc_u32 s11, s11, s37
	ds_read_b128 v[0:3], v72 offset:16384
	s_waitcnt lgkmcnt(3)
	v_mfma_f32_16x16x32_f16 v[56:59], v[12:15], v[22:25], v[44:47]
	v_exp_f32_e32 v106, v48
	v_exp_f32_e32 v107, v49
	v_exp_f32_e32 v110, v50
	v_mfma_f32_16x16x32_f16 v[12:15], v[12:15], v[18:21], v[44:47]
	v_exp_f32_e32 v111, v51
	v_exp_f32_e32 v114, v52
	v_exp_f32_e32 v115, v53
	v_mfma_f32_16x16x32_f16 v[44:47], v[34:37], v[30:33], v[56:59]
	v_mfma_f32_16x16x32_f16 v[56:59], v[34:37], v[26:29], v[12:15]
	ds_read_b128 v[34:37], v72 offset:19456
	ds_read_b128 v[60:63], v71 offset:42944
	s_nop 4
	v_exp_f32_e64 v108, v44 clamp
	ds_read_b128 v[12:15], v72 offset:18432
	s_waitcnt lgkmcnt(3)
	v_mfma_f32_16x16x32_f16 v[64:67], v[0:3], v[22:25], v[8:11]
	v_exp_f32_e64 v109, v45 clamp
	v_exp_f32_e64 v112, v46 clamp
	v_exp_f32_e64 v113, v47 clamp
	v_mfma_f32_16x16x32_f16 v[0:3], v[0:3], v[18:21], v[8:11]
	v_exp_f32_e64 v116, v56 clamp
	v_exp_f32_e64 v117, v57 clamp
	v_exp_f32_e64 v58, v58 clamp
	v_mfma_f32_16x16x32_f16 v[64:67], v[4:7], v[30:33], v[64:67]
	v_exp_f32_e64 v59, v59 clamp
	v_mfma_f32_16x16x32_f16 v[74:77], v[4:7], v[26:29], v[0:3]
	ds_read_b128 v[78:81], v72 offset:20480
	ds_read_b128 v[82:85], v72 offset:21504
	ds_read_b128 v[86:89], v71 offset:43008
	s_waitcnt lgkmcnt(3)
	v_mfma_f32_16x16x32_f16 v[6:9], v[12:15], v[22:25], v[60:63]
	v_mfma_f32_16x16x32_f16 v[60:63], v[12:15], v[18:21], v[60:63]
	v_mfma_f32_16x16x32_f16 v[90:93], v[34:37], v[30:33], v[6:9]
	v_mfma_f32_16x16x32_f16 v[60:63], v[34:37], v[26:29], v[60:63]
	s_nop 1
	ds_read_b128 v[94:97], v72 offset:22528
	ds_read_b128 v[98:101], v72 offset:23552
	ds_read_b128 v[102:105], v71 offset:43072
	s_waitcnt lgkmcnt(3)
	v_mfma_f32_16x16x32_f16 v[44:47], v[78:81], v[22:25], v[86:89]
	v_exp_f32_e32 v0, v64
	v_exp_f32_e32 v1, v65
	v_exp_f32_e32 v34, v66
	v_mfma_f32_16x16x32_f16 v[48:51], v[78:81], v[18:21], v[86:89]
	v_exp_f32_e32 v35, v67
	v_exp_f32_e32 v36, v74
	v_exp_f32_e32 v37, v75
	v_mfma_f32_16x16x32_f16 v[64:67], v[82:85], v[30:33], v[44:47]
	v_exp_f32_e32 v74, v54
	v_exp_f32_e32 v75, v55
	v_exp_f32_e32 v78, v92
	v_mfma_f32_16x16x32_f16 v[50:53], v[82:85], v[26:29], v[48:51]
	v_exp_f32_e32 v44, v76
	v_exp_f32_e32 v45, v77
	v_exp_f32_e32 v76, v90
	s_waitcnt lgkmcnt(0)
	v_mfma_f32_16x16x32_f16 v[46:49], v[94:97], v[22:25], v[102:105]
	v_exp_f32_e32 v77, v91
	v_exp_f32_e64 v64, v64 clamp
	v_exp_f32_e64 v65, v65 clamp
	v_mfma_f32_16x16x32_f16 v[54:57], v[94:97], v[18:21], v[102:105]
	v_exp_f32_e32 v79, v93
	v_exp_f32_e64 v66, v66 clamp
	v_exp_f32_e64 v67, v67 clamp
	v_mfma_f32_16x16x32_f16 v[46:49], v[98:101], v[30:33], v[46:49]
	v_exp_f32_e32 v60, v60
	v_exp_f32_e32 v61, v61
	v_exp_f32_e64 v50, v50 clamp
	v_mfma_f32_16x16x32_f16 v[54:57], v[98:101], v[26:29], v[54:57]
	v_exp_f32_e64 v51, v51 clamp
	s_nop 2
	v_exp_f32_e32 v46, v46
	v_exp_f32_e32 v47, v47
	v_exp_f32_e32 v48, v48
	v_exp_f32_e32 v49, v49
	v_exp_f32_e32 v54, v54
	v_exp_f32_e32 v55, v55
	v_exp_f32_e32 v62, v62
	v_exp_f32_e32 v63, v63
	v_exp_f32_e64 v52, v52 clamp
	v_exp_f32_e64 v53, v53 clamp
	v_exp_f32_e32 v56, v56
	v_exp_f32_e32 v57, v57
	v_pk_fma_f32 v[80:81], v[108:109], s[2:3], 1.0 op_sel_hi:[1,0,0]
	v_pk_fma_f32 v[82:83], v[112:113], s[2:3], 1.0 op_sel_hi:[1,0,0]
	v_pk_fma_f32 v[84:85], v[116:117], s[2:3], 1.0 op_sel_hi:[1,0,0]
	v_pk_fma_f32 v[58:59], v[58:59], s[2:3], 1.0 op_sel_hi:[1,0,0]
	v_pk_fma_f32 v[64:65], v[64:65], s[2:3], 1.0 op_sel_hi:[1,0,0]
	v_pk_fma_f32 v[66:67], v[66:67], s[2:3], 1.0 op_sel_hi:[1,0,0]
	v_pk_fma_f32 v[50:51], v[50:51], s[2:3], 1.0 op_sel_hi:[1,0,0]
	v_pk_fma_f32 v[52:53], v[52:53], s[2:3], 1.0 op_sel_hi:[1,0,0]
	v_pk_fma_f32 v[86:87], v[106:107], v[80:81], v[80:81]
	v_pk_fma_f32 v[88:89], v[110:111], v[82:83], v[82:83]
	v_pk_fma_f32 v[90:91], v[114:115], v[84:85], v[84:85]
	v_pk_fma_f32 v[74:75], v[74:75], v[58:59], v[58:59]
	v_pk_fma_f32 v[76:77], v[76:77], v[64:65], v[64:65]
	v_pk_fma_f32 v[78:79], v[78:79], v[66:67], v[66:67]
	v_pk_fma_f32 v[60:61], v[60:61], v[50:51], v[50:51]
	v_pk_fma_f32 v[62:63], v[62:63], v[52:53], v[52:53]
	v_pk_fma_f32 v[80:81], v[80:81], s[6:7], v[40:41] op_sel_hi:[1,0,0] neg_lo:[1,0,0] neg_hi:[1,0,0]
	v_pk_fma_f32 v[82:83], v[82:83], s[6:7], v[40:41] op_sel_hi:[1,0,0] neg_lo:[1,0,0] neg_hi:[1,0,0]
	v_pk_fma_f32 v[84:85], v[84:85], s[6:7], v[40:41] op_sel_hi:[1,0,0] neg_lo:[1,0,0] neg_hi:[1,0,0]
	v_pk_fma_f32 v[58:59], v[58:59], s[6:7], v[40:41] op_sel_hi:[1,0,0] neg_lo:[1,0,0] neg_hi:[1,0,0]
	v_pk_fma_f32 v[64:65], v[64:65], s[6:7], v[40:41] op_sel_hi:[1,0,0] neg_lo:[1,0,0] neg_hi:[1,0,0]
	v_pk_fma_f32 v[66:67], v[66:67], s[6:7], v[40:41] op_sel_hi:[1,0,0] neg_lo:[1,0,0] neg_hi:[1,0,0]
	v_pk_fma_f32 v[50:51], v[50:51], s[6:7], v[40:41] op_sel_hi:[1,0,0] neg_lo:[1,0,0] neg_hi:[1,0,0]
	v_pk_fma_f32 v[52:53], v[52:53], s[6:7], v[40:41] op_sel_hi:[1,0,0] neg_lo:[1,0,0] neg_hi:[1,0,0]
	v_pk_fma_f32 v[86:87], v[0:1], v[86:87], v[86:87]
	v_pk_fma_f32 v[88:89], v[34:35], v[88:89], v[88:89]
	v_pk_fma_f32 v[90:91], v[36:37], v[90:91], v[90:91]
	v_pk_fma_f32 v[74:75], v[44:45], v[74:75], v[74:75]
	v_pk_fma_f32 v[76:77], v[46:47], v[76:77], v[76:77]
	v_pk_fma_f32 v[78:79], v[48:49], v[78:79], v[78:79]
	v_pk_fma_f32 v[60:61], v[54:55], v[60:61], v[60:61]
	v_pk_fma_f32 v[62:63], v[56:57], v[62:63], v[62:63]
	v_rcp_f32_e64 v86, v86 clamp
	v_rcp_f32_e64 v87, v87 clamp
	v_rcp_f32_e64 v88, v88 clamp
	v_rcp_f32_e64 v89, v89 clamp
	v_rcp_f32_e64 v90, v90 clamp
	v_rcp_f32_e64 v91, v91 clamp
	v_rcp_f32_e64 v74, v74 clamp
	v_rcp_f32_e64 v75, v75 clamp
	v_rcp_f32_e64 v76, v76 clamp
	v_rcp_f32_e64 v77, v77 clamp
	v_rcp_f32_e64 v78, v78 clamp
	v_rcp_f32_e64 v79, v79 clamp
	v_rcp_f32_e64 v60, v60 clamp
	v_rcp_f32_e64 v61, v61 clamp
	v_rcp_f32_e64 v62, v62 clamp
	v_rcp_f32_e64 v63, v63 clamp
	v_pk_mul_f32 v[80:81], v[80:81], v[86:87]
	v_pk_mul_f32 v[82:83], v[82:83], v[88:89]
	v_pk_mul_f32 v[84:85], v[84:85], v[90:91]
	v_pk_mul_f32 v[58:59], v[58:59], v[74:75]
	v_pk_mul_f32 v[64:65], v[64:65], v[76:77]
	v_pk_mul_f32 v[66:67], v[66:67], v[78:79]
	v_pk_mul_f32 v[50:51], v[50:51], v[60:61]
	v_pk_mul_f32 v[60:61], v[52:53], v[62:63]
	v_pk_fma_f32 v[0:1], v[0:1], v[80:81], v[80:81]
	v_pk_fma_f32 v[34:35], v[34:35], v[82:83], v[82:83]
	v_pk_fma_f32 v[36:37], v[36:37], v[84:85], v[84:85]
	v_pk_fma_f32 v[44:45], v[44:45], v[58:59], v[58:59]
	v_pk_fma_f32 v[46:47], v[46:47], v[64:65], v[64:65]
	v_pk_fma_f32 v[48:49], v[48:49], v[66:67], v[66:67]
	v_pk_fma_f32 v[52:53], v[54:55], v[50:51], v[50:51]
	v_pk_fma_f32 v[54:55], v[56:57], v[60:61], v[60:61]
	s_nop 0
	v_pk_fma_f32 v[0:1], v[0:1], v[0:1], s[4:5] neg_lo:[1,0,0] neg_hi:[1,0,0] clamp
	v_pk_fma_f32 v[34:35], v[34:35], v[34:35], s[4:5] neg_lo:[1,0,0] neg_hi:[1,0,0] clamp
	v_pk_fma_f32 v[36:37], v[36:37], v[36:37], s[4:5] neg_lo:[1,0,0] neg_hi:[1,0,0] clamp
	v_pk_fma_f32 v[44:45], v[44:45], v[44:45], s[4:5] neg_lo:[1,0,0] neg_hi:[1,0,0] clamp
	v_pk_fma_f32 v[46:47], v[46:47], v[46:47], s[4:5] neg_lo:[1,0,0] neg_hi:[1,0,0] clamp
	v_pk_fma_f32 v[48:49], v[48:49], v[48:49], s[4:5] neg_lo:[1,0,0] neg_hi:[1,0,0] clamp
	v_pk_fma_f32 v[52:53], v[52:53], v[52:53], s[4:5] neg_lo:[1,0,0] neg_hi:[1,0,0] clamp
	s_nop 0
	v_pk_fma_f32 v[54:55], v[54:55], v[54:55], s[4:5] neg_lo:[1,0,0] neg_hi:[1,0,0] clamp
	s_nop 0
	v_pk_fma_f32 v[0:1], v[0:1], v[0:1], s[8:9] op_sel_hi:[1,1,0]
	v_pk_fma_f32 v[56:57], v[34:35], v[34:35], s[8:9] op_sel_hi:[1,1,0]
	v_pk_fma_f32 v[36:37], v[36:37], v[36:37], s[8:9] op_sel_hi:[1,1,0]
	v_pk_fma_f32 v[44:45], v[44:45], v[44:45], s[8:9] op_sel_hi:[1,1,0]
	v_pk_fma_f32 v[46:47], v[46:47], v[46:47], s[8:9] op_sel_hi:[1,1,0]
	v_pk_fma_f32 v[48:49], v[48:49], v[48:49], s[8:9] op_sel_hi:[1,1,0]
	v_pk_fma_f32 v[62:63], v[52:53], v[52:53], s[8:9] op_sel_hi:[1,1,0]
	v_pk_fma_f32 v[74:75], v[54:55], v[54:55], s[8:9] op_sel_hi:[1,1,0]
	v_pk_mul_f32 v[34:35], v[80:81], v[0:1]
	v_pk_mul_f32 v[56:57], v[82:83], v[56:57]
	v_pk_mul_f32 v[36:37], v[84:85], v[36:37]
	v_pk_mul_f32 v[52:53], v[58:59], v[44:45]
	v_pk_mul_f32 v[54:55], v[64:65], v[46:47]
	v_pk_mul_f32 v[0:1], v[66:67], v[48:49]
	v_pk_mul_f32 v[46:47], v[62:63], v[50:51]
	v_pk_mul_f32 v[44:45], v[60:61], v[74:75]
	ds_read_b128 v[48:51], v72 offset:24576
	ds_read_b128 v[58:61], v71 offset:43136
	ds_read_b128 v[62:65], v72 offset:25600
	ds_read_b128 v[74:77], v72 offset:26624
	ds_read_b128 v[78:81], v72 offset:27648
	ds_read_b128 v[82:85], v71 offset:43200
	v_cvt_pk_f16_f32 v34, v34, v35
	v_cvt_pk_f16_f32 v35, v56, v57
	s_waitcnt lgkmcnt(4)
	v_mfma_f32_16x16x32_f16 v[86:89], v[48:51], v[22:25], v[58:61]
	v_mfma_f32_16x16x32_f16 v[48:51], v[48:51], v[18:21], v[58:61]
	s_waitcnt lgkmcnt(3)
	v_mfma_f32_16x16x32_f16 v[58:61], v[62:65], v[30:33], v[86:89]
	v_mfma_f32_16x16x32_f16 v[86:89], v[62:65], v[26:29], v[48:51]
	ds_read_b128 v[62:65], v72 offset:29696
	ds_read_b128 v[90:93], v71 offset:43264
	s_nop 2
	ds_read_b128 v[48:51], v72 offset:28672
	s_waitcnt lgkmcnt(3)
	v_mfma_f32_16x16x32_f16 v[94:97], v[74:77], v[22:25], v[82:85]
	v_exp_f32_e32 v2, v86
	v_exp_f32_e32 v3, v87
	v_exp_f32_e32 v4, v88
	v_mfma_f32_16x16x32_f16 v[74:77], v[74:77], v[18:21], v[82:85]
	v_exp_f32_e32 v5, v89
	v_mfma_f32_16x16x32_f16 v[82:85], v[78:81], v[30:33], v[94:97]
	v_mfma_f32_16x16x32_f16 v[74:77], v[78:81], v[26:29], v[74:77]
	ds_read_b128 v[78:81], v72 offset:30720
	s_nop 0
	ds_read_b128 v[94:97], v72 offset:31744
	ds_read_b128 v[98:101], v71 offset:43328
	s_waitcnt lgkmcnt(3)
	v_mfma_f32_16x16x32_f16 v[102:105], v[48:51], v[22:25], v[90:93]
	s_nop 0
	v_exp_f32_e64 v66, v82 clamp
	v_exp_f32_e64 v67, v83 clamp
	v_exp_f32_e64 v118, v84 clamp
	v_mfma_f32_16x16x32_f16 v[48:51], v[48:51], v[18:21], v[90:93]
	v_exp_f32_e64 v119, v85 clamp
	v_exp_f32_e64 v6, v74 clamp
	v_exp_f32_e64 v7, v75 clamp
	v_mfma_f32_16x16x32_f16 v[90:93], v[62:65], v[30:33], v[102:105]
	v_exp_f32_e64 v8, v76 clamp
	v_exp_f32_e64 v9, v77 clamp
	v_mfma_f32_16x16x32_f16 v[102:105], v[62:65], v[26:29], v[48:51]
	ds_read_b128 v[106:109], v72 offset:32768
	ds_read_b128 v[110:113], v72 offset:33792
	v_exp_f32_e32 v62, v58
	v_exp_f32_e32 v63, v59
	v_exp_f32_e32 v64, v60
	v_exp_f32_e32 v65, v61
	ds_read_b128 v[114:117], v71 offset:43392
	s_waitcnt lgkmcnt(3)
	v_mfma_f32_16x16x32_f16 v[58:61], v[78:81], v[22:25], v[98:101]
	v_exp_f32_e32 v48, v90
	v_exp_f32_e32 v49, v91
	v_exp_f32_e32 v50, v92
	v_mfma_f32_16x16x32_f16 v[78:81], v[78:81], v[18:21], v[98:101]
	v_exp_f32_e32 v51, v93
	v_mfma_f32_16x16x32_f16 v[82:85], v[94:97], v[30:33], v[58:61]
	v_mfma_f32_16x16x32_f16 v[78:81], v[94:97], v[26:29], v[78:81]
	ds_read_b128 v[86:89], v72 offset:34816
	ds_read_b128 v[90:93], v72 offset:35840
	ds_read_b128 v[94:97], v71 offset:43456
	s_waitcnt lgkmcnt(3)
	v_mfma_f32_16x16x32_f16 v[74:77], v[106:109], v[22:25], v[114:117]
	v_exp_f32_e32 v58, v102
	v_exp_f32_e32 v59, v103
	v_exp_f32_e32 v60, v104
	v_mfma_f32_16x16x32_f16 v[98:101], v[106:109], v[18:21], v[114:117]
	v_exp_f32_e32 v61, v105
	v_exp_f32_e32 v102, v82
	v_exp_f32_e32 v103, v83
	v_exp_f32_e32 v104, v84
	v_exp_f32_e32 v105, v85
	v_mfma_f32_16x16x32_f16 v[74:77], v[110:113], v[30:33], v[74:77]
	v_mfma_f32_16x16x32_f16 v[82:85], v[110:113], v[26:29], v[98:101]
	s_waitcnt lgkmcnt(0)
	v_mfma_f32_16x16x32_f16 v[18:21], v[86:89], v[18:21], v[94:97]
	s_nop 4
	v_exp_f32_e64 v106, v74 clamp
	v_exp_f32_e64 v107, v75 clamp
	v_exp_f32_e64 v108, v76 clamp
	v_exp_f32_e64 v109, v77 clamp
	v_mfma_f32_16x16x32_f16 v[74:77], v[86:89], v[22:25], v[94:97]
	v_cvt_pk_f16_f32 v22, v36, v37
	v_cvt_pk_f16_f32 v23, v52, v53
	v_cvt_pk_f16_f32 v36, v54, v55
	v_mfma_f32_16x16x32_f16 v[18:21], v[90:93], v[26:29], v[18:21]
	v_exp_f32_e32 v52, v78
	v_exp_f32_e32 v53, v79
	v_exp_f32_e64 v54, v82 clamp
	v_mfma_f32_16x16x32_f16 v[30:33], v[90:93], v[30:33], v[74:77]
	v_exp_f32_e64 v55, v83 clamp
	s_nop 2
	v_exp_f32_e32 v18, v18
	v_exp_f32_e32 v19, v19
	v_exp_f32_e32 v26, v80
	v_exp_f32_e32 v27, v81
	v_exp_f32_e32 v30, v30
	v_exp_f32_e32 v31, v31
	v_exp_f32_e32 v32, v32
	v_exp_f32_e32 v33, v33
	v_exp_f32_e64 v28, v84 clamp
	v_exp_f32_e64 v29, v85 clamp
	v_exp_f32_e32 v20, v20
	v_cvt_pk_f16_f32 v24, v46, v47
	v_cvt_pk_f16_f32 v37, v0, v1
	v_cvt_pk_f16_f32 v25, v44, v45
	v_exp_f32_e32 v21, v21
	v_pk_fma_f32 v[0:1], v[66:67], s[2:3], 1.0 op_sel_hi:[1,0,0]
	v_pk_fma_f32 v[44:45], v[118:119], s[2:3], 1.0 op_sel_hi:[1,0,0]
	v_pk_fma_f32 v[46:47], v[6:7], s[2:3], 1.0 op_sel_hi:[1,0,0]
	v_pk_fma_f32 v[56:57], v[8:9], s[2:3], 1.0 op_sel_hi:[1,0,0]
	v_pk_fma_f32 v[66:67], v[106:107], s[2:3], 1.0 op_sel_hi:[1,0,0]
	v_pk_fma_f32 v[74:75], v[108:109], s[2:3], 1.0 op_sel_hi:[1,0,0]
	v_pk_fma_f32 v[54:55], v[54:55], s[2:3], 1.0 op_sel_hi:[1,0,0]
	v_pk_fma_f32 v[28:29], v[28:29], s[2:3], 1.0 op_sel_hi:[1,0,0]
	v_pk_fma_f32 v[62:63], v[62:63], v[0:1], v[0:1]
	v_pk_fma_f32 v[64:65], v[64:65], v[44:45], v[44:45]
	v_pk_fma_f32 v[76:77], v[2:3], v[46:47], v[46:47]
	v_pk_fma_f32 v[78:79], v[4:5], v[56:57], v[56:57]
	v_pk_fma_f32 v[80:81], v[102:103], v[66:67], v[66:67]
	v_pk_fma_f32 v[82:83], v[104:105], v[74:75], v[74:75]
	v_pk_fma_f32 v[52:53], v[52:53], v[54:55], v[54:55]
	v_pk_fma_f32 v[26:27], v[26:27], v[28:29], v[28:29]
	v_pk_fma_f32 v[0:1], v[0:1], s[6:7], v[40:41] op_sel_hi:[1,0,0] neg_lo:[1,0,0] neg_hi:[1,0,0]
	v_pk_fma_f32 v[44:45], v[44:45], s[6:7], v[40:41] op_sel_hi:[1,0,0] neg_lo:[1,0,0] neg_hi:[1,0,0]
	v_pk_fma_f32 v[46:47], v[46:47], s[6:7], v[40:41] op_sel_hi:[1,0,0] neg_lo:[1,0,0] neg_hi:[1,0,0]
	v_pk_fma_f32 v[56:57], v[56:57], s[6:7], v[40:41] op_sel_hi:[1,0,0] neg_lo:[1,0,0] neg_hi:[1,0,0]
	v_pk_fma_f32 v[66:67], v[66:67], s[6:7], v[40:41] op_sel_hi:[1,0,0] neg_lo:[1,0,0] neg_hi:[1,0,0]
	v_pk_fma_f32 v[74:75], v[74:75], s[6:7], v[40:41] op_sel_hi:[1,0,0] neg_lo:[1,0,0] neg_hi:[1,0,0]
	v_pk_fma_f32 v[54:55], v[54:55], s[6:7], v[40:41] op_sel_hi:[1,0,0] neg_lo:[1,0,0] neg_hi:[1,0,0]
	v_pk_fma_f32 v[28:29], v[28:29], s[6:7], v[40:41] op_sel_hi:[1,0,0] neg_lo:[1,0,0] neg_hi:[1,0,0]
	v_pk_fma_f32 v[62:63], v[48:49], v[62:63], v[62:63]
	v_pk_fma_f32 v[64:65], v[50:51], v[64:65], v[64:65]
	v_pk_fma_f32 v[76:77], v[58:59], v[76:77], v[76:77]
	v_pk_fma_f32 v[78:79], v[60:61], v[78:79], v[78:79]
	v_pk_fma_f32 v[80:81], v[30:31], v[80:81], v[80:81]
	v_pk_fma_f32 v[82:83], v[32:33], v[82:83], v[82:83]
	v_pk_fma_f32 v[52:53], v[18:19], v[52:53], v[52:53]
	v_pk_fma_f32 v[26:27], v[20:21], v[26:27], v[26:27]
	global_load_dwordx4 v[10:13], v39, s[10:11] offset:16
	global_load_dwordx4 v[14:17], v39, s[10:11]
	global_load_dwordx4 v[2:5], v39, s[10:11] offset:2064
	global_load_dwordx4 v[6:9], v39, s[10:11] offset:2048
	v_rcp_f32_e64 v62, v62 clamp
	v_rcp_f32_e64 v63, v63 clamp
	v_rcp_f32_e64 v64, v64 clamp
	v_rcp_f32_e64 v65, v65 clamp
	v_rcp_f32_e64 v76, v76 clamp
	v_rcp_f32_e64 v77, v77 clamp
	v_rcp_f32_e64 v78, v78 clamp
	v_rcp_f32_e64 v79, v79 clamp
	v_rcp_f32_e64 v80, v80 clamp
	v_rcp_f32_e64 v81, v81 clamp
	v_rcp_f32_e64 v82, v82 clamp
	v_rcp_f32_e64 v83, v83 clamp
	v_rcp_f32_e64 v52, v52 clamp
	v_rcp_f32_e64 v53, v53 clamp
	v_rcp_f32_e64 v26, v26 clamp
	v_rcp_f32_e64 v27, v27 clamp
	v_pk_mul_f32 v[52:53], v[54:55], v[52:53]
	v_pk_mul_f32 v[0:1], v[0:1], v[62:63]
	v_pk_mul_f32 v[44:45], v[44:45], v[64:65]
	v_pk_mul_f32 v[46:47], v[46:47], v[76:77]
	v_pk_mul_f32 v[56:57], v[56:57], v[78:79]
	v_pk_mul_f32 v[62:63], v[66:67], v[80:81]
	v_pk_mul_f32 v[64:65], v[74:75], v[82:83]
	v_pk_mul_f32 v[26:27], v[28:29], v[26:27]
	v_pk_fma_f32 v[18:19], v[18:19], v[52:53], v[52:53]
	v_pk_fma_f32 v[28:29], v[48:49], v[0:1], v[0:1]
	v_pk_fma_f32 v[48:49], v[50:51], v[44:45], v[44:45]
	v_pk_fma_f32 v[50:51], v[58:59], v[46:47], v[46:47]
	v_pk_fma_f32 v[54:55], v[60:61], v[56:57], v[56:57]
	v_pk_fma_f32 v[30:31], v[30:31], v[62:63], v[62:63]
	v_pk_fma_f32 v[32:33], v[32:33], v[64:65], v[64:65]
	v_pk_fma_f32 v[20:21], v[20:21], v[26:27], v[26:27]
	s_nop 0
	v_pk_fma_f32 v[28:29], v[28:29], v[28:29], s[4:5] neg_lo:[1,0,0] neg_hi:[1,0,0] clamp
	v_pk_fma_f32 v[48:49], v[48:49], v[48:49], s[4:5] neg_lo:[1,0,0] neg_hi:[1,0,0] clamp
	v_pk_fma_f32 v[50:51], v[50:51], v[50:51], s[4:5] neg_lo:[1,0,0] neg_hi:[1,0,0] clamp
	v_pk_fma_f32 v[54:55], v[54:55], v[54:55], s[4:5] neg_lo:[1,0,0] neg_hi:[1,0,0] clamp
	v_pk_fma_f32 v[30:31], v[30:31], v[30:31], s[4:5] neg_lo:[1,0,0] neg_hi:[1,0,0] clamp
	v_pk_fma_f32 v[32:33], v[32:33], v[32:33], s[4:5] neg_lo:[1,0,0] neg_hi:[1,0,0] clamp
	v_pk_fma_f32 v[18:19], v[18:19], v[18:19], s[4:5] neg_lo:[1,0,0] neg_hi:[1,0,0] clamp
	s_nop 0
	v_pk_fma_f32 v[20:21], v[20:21], v[20:21], s[4:5] neg_lo:[1,0,0] neg_hi:[1,0,0] clamp
	s_nop 0
	v_pk_fma_f32 v[28:29], v[28:29], v[28:29], s[8:9] op_sel_hi:[1,1,0]
	v_pk_fma_f32 v[48:49], v[48:49], v[48:49], s[8:9] op_sel_hi:[1,1,0]
	v_pk_fma_f32 v[50:51], v[50:51], v[50:51], s[8:9] op_sel_hi:[1,1,0]
	v_pk_fma_f32 v[54:55], v[54:55], v[54:55], s[8:9] op_sel_hi:[1,1,0]
	v_pk_fma_f32 v[30:31], v[30:31], v[30:31], s[8:9] op_sel_hi:[1,1,0]
	v_pk_fma_f32 v[32:33], v[32:33], v[32:33], s[8:9] op_sel_hi:[1,1,0]
	v_pk_fma_f32 v[18:19], v[18:19], v[18:19], s[8:9] op_sel_hi:[1,1,0]
	v_pk_fma_f32 v[20:21], v[20:21], v[20:21], s[8:9] op_sel_hi:[1,1,0]
	v_pk_mul_f32 v[0:1], v[0:1], v[28:29]
	v_pk_mul_f32 v[58:59], v[44:45], v[48:49]
	v_pk_mul_f32 v[60:61], v[46:47], v[50:51]
	v_pk_mul_f32 v[54:55], v[56:57], v[54:55]
	v_pk_mul_f32 v[62:63], v[62:63], v[30:31]
	v_pk_mul_f32 v[64:65], v[64:65], v[32:33]
	v_pk_mul_f32 v[66:67], v[18:19], v[52:53]
	v_pk_mul_f32 v[74:75], v[26:27], v[20:21]
	ds_read_b128 v[18:21], v72 offset:36864
	ds_read_b128 v[30:33], v72 offset:37888
	ds_read_b128 v[26:29], v71 offset:43520
	v_cvt_pk_f16_f32 v56, v60, v61
	v_cvt_pk_f16_f32 v57, v54, v55
	v_cvt_pk_f16_f32 v54, v62, v63
	ds_read_b128 v[60:63], v71 offset:43584
	v_cvt_pk_f16_f32 v52, v0, v1
	v_cvt_pk_f16_f32 v53, v58, v59
	s_waitcnt lgkmcnt(1)
	v_mfma_f32_16x16x32_f16 v[48:51], v[18:21], v[34:37], v[26:29]
	v_cvt_pk_f16_f32 v55, v64, v65
	v_cvt_pk_f16_f32 v58, v66, v67
	v_cvt_pk_f16_f32 v59, v74, v75
	v_mfma_f32_16x16x32_f16 v[18:21], v[18:21], v[22:25], v[26:29]
	ds_read_b128 v[44:47], v72 offset:40960
	s_add_i32 s12, s12, s3
	s_add_i32 s10, s20, s12
	v_mfma_f32_16x16x32_f16 v[26:29], v[30:33], v[52:55], v[48:51]
	s_cmp_lt_i32 s10, 0x8000
	v_add_u32_e32 v38, s7, v38
	s_nop 0
	ds_read_b128 v[48:51], v72 offset:38912
	v_mfma_f32_16x16x32_f16 v[18:21], v[30:33], v[56:59], v[18:21]
	ds_read_b128 v[30:33], v72 offset:39936
	s_nop 1
	v_cvt_pk_f16_f32 v1, v28, v29
	v_cvt_pk_f16_f32 v0, v26, v27
	s_waitcnt lgkmcnt(1)
	v_mfma_f32_16x16x32_f16 v[34:37], v[48:51], v[34:37], v[60:63]
	v_pk_max_f16 v27, v1, 0
	v_cvt_pk_f16_f32 v1, v20, v21
	v_pk_max_f16 v26, v0, 0
	v_mfma_f32_16x16x32_f16 v[20:23], v[48:51], v[22:25], v[60:63]
	v_cvt_pk_f16_f32 v0, v18, v19
	v_pk_max_f16 v18, v0, 0
	v_pk_max_f16 v19, v1, 0
	s_waitcnt lgkmcnt(0)
	v_mfma_f32_16x16x32_f16 v[34:37], v[30:33], v[52:55], v[34:37]
	v_mfma_f32_16x16x32_f16 v[20:23], v[30:33], v[56:59], v[20:23]
	s_nop 6
	v_cvt_pk_f16_f32 v0, v34, v35
	v_cvt_pk_f16_f32 v1, v36, v37
	v_pk_max_f16 v28, v0, 0
	v_pk_max_f16 v29, v1, 0
	v_cvt_pk_f16_f32 v0, v20, v21
	v_cvt_pk_f16_f32 v1, v22, v23
	v_pk_max_f16 v20, v0, 0
	v_pk_max_f16 v21, v1, 0
	v_mfma_f32_16x16x32_f16 v[24:27], v[44:47], v[26:29], 0
	s_nop 0
	v_mfma_f32_16x16x32_f16 v[18:21], v[44:47], v[18:21], 0
	s_nop 7
	v_cndmask_b32_e64 v18, v24, v18, s[0:1]
	s_cbranch_scc0 .LBB0_37
